# variant: iteration slot table stored with default policy (stays in L2 for the next launch), other first-kernel tables written through
# baseline (speedup 1.0000x reference)
.Lb3_top:
	v_add_u32_e32 v216, s61, v0
	v_add_u32_e32 v217, 0x200, v216
	v_add_u32_e32 v218, 0x400, v216
	v_cmp_gt_i32_e64 s[66:67], s60, v216
	v_cmp_gt_i32_e64 s[68:69], s60, v217
	v_cmp_gt_i32_e64 s[70:71], s60, v218
	v_add_u32_e32 v220, 64, v9
	v_add_u32_e32 v221, 0x80, v9
	v_cndmask_b32_e64 v219, 0, v9, s[66:67]
	v_cndmask_b32_e64 v220, 0, v220, s[68:69]
	v_cndmask_b32_e64 v221, 0, v221, s[70:71]
	v_lshlrev_b32_e32 v219, 2, v219
	v_lshlrev_b32_e32 v220, 2, v220
	v_lshlrev_b32_e32 v221, 2, v221
	ds_read_b32 v219, v219 offset:24576
	ds_read_b32 v220, v220 offset:24576
	ds_read_b32 v221, v221 offset:24576
	s_waitcnt lgkmcnt(0)
	v_lshl_or_b32 v219, v219, 3, v5
	v_lshl_or_b32 v220, v220, 3, v5
	v_lshl_or_b32 v221, v221, 3, v5
	v_add_lshl_u32 v222, v219, s58, 2
	v_add_lshl_u32 v223, v220, s58, 2
	v_add_lshl_u32 v224, v221, s58, 2
	global_load_dword v226, v222, s[40:41]
	global_load_dword v227, v222, s[42:43]
	global_load_dword v228, v222, s[52:53]
	global_load_dword v230, v223, s[40:41]
	global_load_dword v231, v223, s[42:43]
	global_load_dword v232, v223, s[52:53]
	global_load_dword v234, v224, s[40:41]
	global_load_dword v235, v224, s[42:43]
	global_load_dword v236, v224, s[52:53]
	v_lshlrev_b32_e32 v216, 4, v216
	v_lshlrev_b32_e32 v217, 4, v217
	v_lshlrev_b32_e32 v218, 4, v218
	s_waitcnt vmcnt(0)
	v_pk_add_f32 v[238:239], v[226:227], v[22:23] neg_lo:[0,1] neg_hi:[0,1]
	v_mov_b32_e32 v241, v219
	v_pk_mul_f32 v[250:251], v[238:239], v[238:239]
	v_cmp_ne_u32_e64 s[72:73], 0, v228
	v_sub_f32_e32 v252, s36, v226
	v_add_f32_e32 v240, v250, v251
	v_mul_f32_e32 v240, 0xc31044f5, v240
	v_cndmask_b32_e64 v240, v30, v240, s[72:73]
	s_mov_b64 exec, s[66:67]
	global_store_dwordx4 v216, v[238:241], s[20:21] sc1
	s_mov_b64 exec, -1
	v_subrev_f32_e32 v253, s38, v226
	v_max3_f32 v252, v252, v253, 0
	v_sub_f32_e32 v253, s37, v227
	v_subrev_f32_e32 v254, s39, v227
	v_max3_f32 v253, v253, v254, 0
	v_pk_mul_f32 v[252:253], v[252:253], v[252:253]
	s_nop 0
	v_add_f32_e32 v252, v252, v253
	v_cmp_gt_f32_e64 s[74:75], s62, v252
	s_and_b64 s[72:73], s[72:73], s[74:75]
	s_and_b64 s[76:77], s[66:67], s[72:73]
	s_bcnt1_i32_b64 s82, s[76:77]
	v_pk_add_f32 v[242:243], v[230:231], v[22:23] neg_lo:[0,1] neg_hi:[0,1]
	v_mov_b32_e32 v245, v220
	v_pk_mul_f32 v[250:251], v[242:243], v[242:243]
	v_cmp_ne_u32_e64 s[72:73], 0, v232
	v_sub_f32_e32 v252, s36, v230
	v_add_f32_e32 v244, v250, v251
	v_mul_f32_e32 v244, 0xc31044f5, v244
	v_cndmask_b32_e64 v244, v30, v244, s[72:73]
	s_mov_b64 exec, s[68:69]
	global_store_dwordx4 v217, v[242:245], s[20:21] sc1
	s_mov_b64 exec, -1
	v_subrev_f32_e32 v253, s38, v230
	v_max3_f32 v252, v252, v253, 0
	v_sub_f32_e32 v253, s37, v231
	v_subrev_f32_e32 v254, s39, v231
	v_max3_f32 v253, v253, v254, 0
	v_pk_mul_f32 v[252:253], v[252:253], v[252:253]
	s_nop 0
	v_add_f32_e32 v252, v252, v253
	v_cmp_gt_f32_e64 s[74:75], s62, v252
	s_and_b64 s[72:73], s[72:73], s[74:75]
	s_and_b64 s[78:79], s[68:69], s[72:73]
	s_bcnt1_i32_b64 s83, s[78:79]
	v_pk_add_f32 v[246:247], v[234:235], v[22:23] neg_lo:[0,1] neg_hi:[0,1]
	v_mov_b32_e32 v249, v221
	v_pk_mul_f32 v[250:251], v[246:247], v[246:247]
	v_cmp_ne_u32_e64 s[72:73], 0, v236
	v_sub_f32_e32 v252, s36, v234
	v_add_f32_e32 v248, v250, v251
	v_mul_f32_e32 v248, 0xc31044f5, v248
	v_cndmask_b32_e64 v248, v30, v248, s[72:73]
	s_mov_b64 exec, s[70:71]
	global_store_dwordx4 v218, v[246:249], s[20:21] sc1
	s_mov_b64 exec, -1
	v_subrev_f32_e32 v253, s38, v234
	v_max3_f32 v252, v252, v253, 0
	v_sub_f32_e32 v253, s37, v235
	v_subrev_f32_e32 v254, s39, v235
	v_max3_f32 v253, v253, v254, 0
	v_pk_mul_f32 v[252:253], v[252:253], v[252:253]
	s_nop 0
	v_add_f32_e32 v252, v252, v253
	v_cmp_gt_f32_e64 s[74:75], s62, v252
	s_and_b64 s[72:73], s[72:73], s[74:75]
	s_and_b64 s[80:81], s[70:71], s[72:73]
	s_bcnt1_i32_b64 s84, s[80:81]
	v_mov_b32_e32 v250, s82
	v_mov_b32_e32 v251, s83
	v_mov_b32_e32 v252, s84
	v_mov_b32_e32 v253, s47
	s_and_saveexec_b64 s[22:23], vcc
	ds_write_b32 v253, v250 offset:3104
	ds_write_b32 v253, v251 offset:3136
	ds_write_b32 v253, v252 offset:3168
	s_or_b64 exec, exec, s[22:23]
	s_waitcnt lgkmcnt(0)
	s_barrier
	v_lshlrev_b32_e32 v250, 2, v44
	ds_read_b32 v250, v250 offset:27680
	v_cmp_gt_u32_e64 s[72:73], 24, v44
	s_add_i32 s85, s27, 8
	s_add_i32 s86, s27, 16
	s_waitcnt lgkmcnt(0)
	v_cndmask_b32_e64 v250, 0, v250, s[72:73]
	s_nop 1
	v_add_u32_dpp v251, v250, v250 row_shr:1 row_mask:0xf bank_mask:0xf bound_ctrl:1
	s_nop 1
	v_add_u32_dpp v251, v251, v251 row_shr:2 row_mask:0xf bank_mask:0xf bound_ctrl:1
	s_nop 1
	v_add_u32_dpp v251, v251, v251 row_shr:4 row_mask:0xf bank_mask:0xf bound_ctrl:1
	s_nop 1
	v_add_u32_dpp v251, v251, v251 row_shr:8 row_mask:0xf bank_mask:0xf bound_ctrl:1
	s_nop 1
	v_add_u32_dpp v251, v251, v251 row_bcast:15 row_mask:0xa bank_mask:0xf
	v_sub_u32_e32 v252, v251, v250
	s_nop 1
	v_readlane_b32 s87, v252, s27
	v_readlane_b32 s88, v252, s85
	v_readlane_b32 s89, v252, s86
	v_readlane_b32 s90, v251, 23
	s_nop 1
	s_add_i32 s87, s87, s91
	v_mbcnt_lo_u32_b32 v253, s76, 0
	v_mbcnt_hi_u32_b32 v253, s77, v253
	v_add_u32_e32 v253, s87, v253
	v_lshlrev_b32_e32 v254, 4, v253
	v_cmp_gt_u32_e64 s[72:73], s63, v253
	s_mov_b64 exec, s[76:77]
	global_store_dwordx4 v254, v[238:241], s[44:45]
	s_and_b64 exec, exec, s[72:73]
	ds_write_b128 v254, v[238:241]
	s_mov_b64 exec, -1
	s_add_i32 s88, s88, s91
	v_mbcnt_lo_u32_b32 v253, s78, 0
	v_mbcnt_hi_u32_b32 v253, s79, v253
	v_add_u32_e32 v253, s88, v253
	v_lshlrev_b32_e32 v254, 4, v253
	v_cmp_gt_u32_e64 s[72:73], s63, v253
	s_mov_b64 exec, s[78:79]
	global_store_dwordx4 v254, v[242:245], s[44:45]
	s_and_b64 exec, exec, s[72:73]
	ds_write_b128 v254, v[242:245]
	s_mov_b64 exec, -1
	s_add_i32 s89, s89, s91
	v_mbcnt_lo_u32_b32 v253, s80, 0
	v_mbcnt_hi_u32_b32 v253, s81, v253
	v_add_u32_e32 v253, s89, v253
	v_lshlrev_b32_e32 v254, 4, v253
	v_cmp_gt_u32_e64 s[72:73], s63, v253
	s_mov_b64 exec, s[80:81]
	global_store_dwordx4 v254, v[246:249], s[44:45]
	s_and_b64 exec, exec, s[72:73]
	ds_write_b128 v254, v[246:249]
	s_mov_b64 exec, -1
	s_add_i32 s91, s91, s90
	s_addk_i32 s61, 0x600
	v_add_u32_e32 v9, 0xc0, v9
	s_cmp_ge_i32 s61, s60
	s_waitcnt lgkmcnt(0)
	s_barrier
	s_cbranch_scc0 .Lb3_top
	v_mov_b32_e32 v6, s91
	s_branch .LBB2_21
